# baseline (speedup 1.0000x reference)
_Z11pam_combinePKDF16_PKfS2_S2_Pf:
	s_load_dwordx8 s[8:15], s[0:1], 0x0
	s_load_dwordx2 s[20:21], s[0:1], 0x20
	v_lshl_or_b32 v0, s2, 8, v0
	s_mov_b32 s2, 0x1f800
	v_cmp_gt_i32_e32 vcc, s2, v0
	s_and_saveexec_b64 s[2:3], vcc
	s_cbranch_execz .LBB2_3
	s_mov_b32 s2, 0x92492493
	v_mul_hi_i32 v1, v0, s2
	v_add_u32_e32 v1, v1, v0
	v_lshrrev_b32_e32 v2, 31, v1
	v_ashrrev_i32_e32 v1, 2, v1
	s_mov_b32 s2, 0x30c30c31
	v_add_u32_e32 v35, v1, v2
	v_mul_hi_i32 v1, v0, s2
	v_lshrrev_b32_e32 v2, 31, v1
	v_ashrrev_i32_e32 v1, 9, v1
	v_add_u32_e32 v1, v1, v2
	v_mul_i32_i24_e32 v2, 0x120, v1
	s_mov_b32 s3, 0x4bda12f7
	v_mul_hi_i32 v2, v2, s3
	s_movk_i32 s2, 0xfe80
	v_lshrrev_b32_e32 v3, 31, v2
	v_ashrrev_i32_e32 v2, 4, v2
	v_mad_i32_i24 v20, v1, s2, v35
	s_movk_i32 s2, 0x120
	v_add_u32_e32 v14, v2, v3
	v_mov_b32_e32 v2, 0x11f
	v_mad_i32_i24 v2, v1, s2, v2
	v_mul_hi_i32 v2, v2, s3
	v_lshrrev_b32_e32 v3, 31, v2
	v_ashrrev_i32_e32 v2, 4, v2
	v_add_u32_e32 v2, v2, v3
	v_sub_u32_e32 v34, v2, v14
	v_min_i32_e32 v2, 0, v34
	v_add_u32_e32 v2, v2, v14
	v_mul_lo_u32 v3, v2, 54
	s_mov_b32 s4, 0x38e38e39
	v_mul_hi_i32 v3, v3, s4
	v_lshrrev_b32_e32 v4, 31, v3
	v_ashrrev_i32_e32 v3, 6, v3
	v_add_u32_e32 v3, v3, v4
	v_min_i32_e32 v4, 1, v34
	v_add_u32_e32 v4, v4, v14
	v_mul_lo_u32 v5, v4, 54
	v_mul_hi_i32 v5, v5, s4
	v_lshrrev_b32_e32 v6, 31, v5
	v_ashrrev_i32_e32 v5, 6, v5
	v_add_u32_e32 v5, v5, v6
	v_min_i32_e32 v6, 2, v34
	v_add_u32_e32 v6, v6, v14
	v_mul_lo_u32 v7, v6, 54
	v_mul_hi_i32 v7, v7, s4
	v_lshrrev_b32_e32 v8, 31, v7
	v_ashrrev_i32_e32 v7, 6, v7
	v_add_u32_e32 v7, v7, v8
	v_min_i32_e32 v8, 3, v34
	v_add_u32_e32 v8, v8, v14
	v_mul_lo_u32 v9, v8, 54
	v_mul_hi_i32 v9, v9, s4
	v_lshrrev_b32_e32 v10, 31, v9
	v_ashrrev_i32_e32 v9, 6, v9
	v_add_u32_e32 v9, v9, v10
	v_min_i32_e32 v10, 4, v34
	v_add_u32_e32 v10, v10, v14
	v_mul_lo_u32 v11, v10, 54
	v_mul_hi_i32 v11, v11, s4
	v_lshrrev_b32_e32 v12, 31, v11
	v_ashrrev_i32_e32 v11, 6, v11
	v_add_u32_e32 v11, v11, v12
	v_min_i32_e32 v12, 5, v34
	v_add_u32_e32 v15, 0x100, v1
	v_cmp_eq_u32_e32 vcc, v3, v1
	v_add_u32_e32 v12, v12, v14
	v_mul_lo_u32 v13, v12, 54
	v_cndmask_b32_e32 v16, v15, v2, vcc
	v_cmp_eq_u32_e32 vcc, v5, v1
	v_mul_hi_i32 v13, v13, s4
	v_cndmask_b32_e32 v17, v15, v4, vcc
	v_cmp_eq_u32_e32 vcc, v7, v1
	v_lshrrev_b32_e32 v22, 31, v13
	v_ashrrev_i32_e32 v13, 6, v13
	v_cndmask_b32_e32 v18, v15, v6, vcc
	v_cmp_eq_u32_e32 vcc, v9, v1
	v_add_u32_e32 v13, v13, v22
	v_ashrrev_i32_e32 v21, 31, v20
	v_cndmask_b32_e32 v19, v15, v8, vcc
	v_cmp_eq_u32_e32 vcc, v11, v1
	s_movk_i32 s5, 0x180
	v_mad_u64_u32 v[4:5], s[2:3], v17, s5, v[20:21]
	v_cndmask_b32_e32 v26, v15, v10, vcc
	v_cmp_eq_u32_e32 vcc, v13, v1
	v_ashrrev_i32_e32 v5, 31, v4
	v_mad_u64_u32 v[6:7], s[2:3], v18, s5, v[20:21]
	v_cndmask_b32_e32 v30, v15, v12, vcc
	v_mad_u64_u32 v[8:9], s[2:3], v19, s5, v[20:21]
	v_mad_u64_u32 v[10:11], s[2:3], v26, s5, v[20:21]
	v_mad_u64_u32 v[12:13], s[2:3], v30, s5, v[20:21]
	s_waitcnt lgkmcnt(0)
	s_load_dword s18, s[14:15], 0x0
	v_mad_i32_i24 v68, v35, -7, v0
	v_mul_u32_u24_e32 v69, 0xc8, v35
	v_cmp_gt_i32_e32 vcc, 6, v68
	v_lshl_add_u32 v69, v68, 5, v69
	v_cndmask_b32_e64 v76, 0, 8, vcc
	global_load_dwordx2 v[70:71], v69, s[12:13]
	v_add_u32_e32 v77, v69, v76
	v_lshl_add_u32 v78, v76, 1, v69
	v_mad_u32_u24 v79, v76, 3, v69
	global_load_dwordx2 v[72:73], v77, s[12:13]
	global_load_dwordx2 v[74:75], v78, s[12:13]
	global_load_dwordx2 v[80:81], v79, s[12:13]
	v_lshl_add_u64 v[4:5], v[4:5], 2, s[10:11]
	v_ashrrev_i32_e32 v7, 31, v6
	v_ashrrev_i32_e32 v9, 31, v8
	v_ashrrev_i32_e32 v11, 31, v10
	v_ashrrev_i32_e32 v13, 31, v12
	v_lshl_add_u64 v[6:7], v[6:7], 2, s[10:11]
	v_lshl_add_u64 v[8:9], v[8:9], 2, s[10:11]
	v_lshl_add_u64 v[10:11], v[10:11], 2, s[10:11]
	v_lshl_add_u64 v[12:13], v[12:13], 2, s[10:11]
	global_load_dword v36, v[4:5], off
	global_load_dword v37, v[6:7], off
	global_load_dword v38, v[8:9], off
	global_load_dword v39, v[10:11], off
	global_load_dword v41, v[12:13], off
	v_min_i32_e32 v4, 6, v34
	v_add_u32_e32 v4, v4, v14
	v_mul_lo_u32 v5, v4, 54
	v_mul_hi_i32 v5, v5, s4
	v_lshrrev_b32_e32 v6, 31, v5
	v_ashrrev_i32_e32 v5, 6, v5
	v_add_u32_e32 v5, v5, v6
	v_cmp_eq_u32_e32 vcc, v5, v1
	v_mad_u64_u32 v[2:3], s[2:3], v16, s5, v[20:21]
	s_nop 0
	v_cndmask_b32_e32 v32, v15, v4, vcc
	v_mad_u64_u32 v[4:5], s[2:3], v32, s5, v[20:21]
	v_ashrrev_i32_e32 v5, 31, v4
	v_ashrrev_i32_e32 v3, 31, v2
	v_lshl_add_u64 v[4:5], v[4:5], 2, s[10:11]
	v_lshl_add_u64 v[2:3], v[2:3], 2, s[10:11]
	global_load_dword v43, v[4:5], off
	global_load_dword v40, v[2:3], off
	v_mad_u64_u32 v[44:45], s[2:3], v35, -7, v[0:1]
	v_lshlrev_b32_e32 v28, 3, v44
	v_ashrrev_i32_e32 v29, 31, v28
	v_lshl_add_u64 v[22:23], v[28:29], 1, s[8:9]
	v_mad_i64_i32 v[0:1], s[2:3], v16, s5, v[20:21]
	s_movk_i32 s4, 0x68
	v_mad_u64_u32 v[2:3], s[2:3], v0, s4, v[22:23]
	v_mad_i64_i32 v[4:5], s[2:3], v17, s5, v[20:21]
	v_mad_i32_i24 v3, v1, s4, v3
	v_mad_u64_u32 v[12:13], s[2:3], v4, s4, v[22:23]
	global_load_dwordx4 v[0:3], v[2:3], off nt
	v_mad_i32_i24 v13, v5, s4, v13
	v_mad_i64_i32 v[4:5], s[2:3], v18, s5, v[20:21]
	v_mad_u64_u32 v[14:15], s[2:3], v4, s4, v[22:23]
	v_mad_i32_i24 v15, v5, s4, v15
	global_load_dwordx4 v[4:7], v[12:13], off nt
	global_load_dwordx4 v[8:11], v[14:15], off nt
	v_mad_i64_i32 v[12:13], s[2:3], v19, s5, v[20:21]
	v_mad_u64_u32 v[24:25], s[2:3], v12, s4, v[22:23]
	v_mad_i32_i24 v25, v13, s4, v25
	v_mad_i64_i32 v[12:13], s[2:3], v26, s5, v[20:21]
	v_mad_u64_u32 v[26:27], s[2:3], v12, s4, v[22:23]
	v_mad_i32_i24 v27, v13, s4, v27
	global_load_dwordx4 v[12:15], v[24:25], off nt
	global_load_dwordx4 v[16:19], v[26:27], off nt
	v_mad_i64_i32 v[24:25], s[2:3], v30, s5, v[20:21]
	v_mad_u64_u32 v[30:31], s[2:3], v24, s4, v[22:23]
	v_mad_i64_i32 v[20:21], s[2:3], v32, s5, v[20:21]
	v_mad_i32_i24 v31, v25, s4, v31
	v_mad_u64_u32 v[32:33], s[2:3], v20, s4, v[22:23]
	v_mad_i32_i24 v33, v21, s4, v33
	global_load_dwordx4 v[20:23], v[30:31], off nt
	global_load_dwordx4 v[24:27], v[32:33], off nt
	s_movk_i32 s16, 0xc8
	v_mov_b64_e32 v[30:31], s[12:13]
	v_mad_i64_i32 v[30:31], s[2:3], v35, s16, v[30:31]
	v_lshlrev_b64 v[46:47], 2, v[28:29]
	v_lshl_add_u64 v[28:29], v[30:31], 0, v[46:47]
	v_mov_b32_e32 v30, 0xff61b1e6
	v_cmp_gt_i32_e32 vcc, 1, v34
	v_cmp_gt_i32_e64 s[2:3], 2, v34
	v_cmp_gt_i32_e64 s[4:5], 3, v34
	v_cmp_gt_i32_e64 s[6:7], 4, v34
	v_cmp_gt_i32_e64 s[8:9], 5, v34
	v_cmp_gt_i32_e64 s[10:11], 6, v34
	v_cmp_gt_i32_e64 s[12:13], 0, v34
	s_waitcnt vmcnt(13)
	v_cndmask_b32_e32 v31, v36, v30, vcc
	s_waitcnt vmcnt(12)
	v_cndmask_b32_e64 v32, v37, v30, s[2:3]
	s_waitcnt vmcnt(11)
	v_cndmask_b32_e64 v33, v38, v30, s[4:5]
	s_waitcnt vmcnt(10)
	v_cndmask_b32_e64 v42, v39, v30, s[6:7]
	s_waitcnt vmcnt(9)
	v_cndmask_b32_e64 v45, v41, v30, s[8:9]
	s_waitcnt vmcnt(8)
	v_cndmask_b32_e64 v50, v43, v30, s[10:11]
	s_waitcnt vmcnt(7)
	v_max_f32_e32 v48, v40, v40
	v_max_f32_e32 v51, 0xff61b1e6, v48
	v_cndmask_b32_e64 v30, v51, v30, s[12:13]
	v_max3_f32 v30, v30, v31, v32
	v_max3_f32 v30, v30, v33, v42
	v_max3_f32 v30, v30, v45, v50
	v_sub_f32_e32 v31, v40, v30
	v_exp_f32_e32 v31, v31
	v_sub_f32_e32 v32, v37, v30
	v_exp_f32_e32 v32, v32
	v_cndmask_b32_e64 v42, v31, 0, s[12:13]
	v_sub_f32_e32 v31, v36, v30
	v_exp_f32_e32 v31, v31
	v_cndmask_b32_e64 v34, v32, 0, s[2:3]
	v_sub_f32_e32 v32, v38, v30
	v_add_f32_e32 v33, 0, v42
	v_cndmask_b32_e64 v36, v31, 0, vcc
	v_exp_f32_e32 v32, v32
	v_add_f32_e32 v31, v33, v36
	v_sub_f32_e32 v33, v39, v30
	v_exp_f32_e32 v33, v33
	v_cndmask_b32_e64 v40, v32, 0, s[4:5]
	v_sub_f32_e32 v32, v41, v30
	v_exp_f32_e32 v32, v32
	v_sub_f32_e32 v30, v43, v30
	v_cndmask_b32_e64 v38, v33, 0, s[6:7]
	v_exp_f32_e32 v33, v30
	v_add_f32_e32 v31, v31, v34
	v_add_f32_e32 v31, v31, v40
	v_add_f32_e32 v31, v31, v38
	v_cndmask_b32_e64 v30, v32, 0, s[8:9]
	v_add_f32_e32 v31, v31, v30
	v_cndmask_b32_e64 v32, v33, 0, s[10:11]
	v_add_f32_e32 v31, v31, v32
	v_div_scale_f32 v33, s[2:3], v31, v31, 1.0
	v_rcp_f32_e32 v37, v33
	s_waitcnt vmcnt(6)
	v_cvt_f32_f16_e32 v56, v0
	v_cvt_f32_f16_sdwa v57, v0 dst_sel:DWORD dst_unused:UNUSED_PAD src0_sel:WORD_1
	s_waitcnt vmcnt(5)
	v_cvt_f32_f16_e32 v54, v4
	v_fma_f32 v39, -v33, v37, 1.0
	v_fmac_f32_e32 v37, v39, v37
	v_div_scale_f32 v39, vcc, 1.0, v31, 1.0
	v_cvt_f32_f16_sdwa v55, v4 dst_sel:DWORD dst_unused:UNUSED_PAD src0_sel:WORD_1
	v_mul_f32_e32 v41, v39, v37
	s_waitcnt vmcnt(4)
	v_cvt_f32_f16_e32 v58, v8
	v_cvt_f32_f16_sdwa v59, v8 dst_sel:DWORD dst_unused:UNUSED_PAD src0_sel:WORD_1
	v_fma_f32 v43, -v33, v41, v39
	v_pk_fma_f32 v[56:57], v[42:43], v[56:57], 0 op_sel_hi:[0,1,0]
	v_pk_fma_f32 v[54:55], v[36:37], v[54:55], v[56:57] op_sel_hi:[0,1,1]
	v_pk_fma_f32 v[54:55], v[34:35], v[58:59], v[54:55] op_sel_hi:[0,1,1]
	s_waitcnt vmcnt(3)
	v_cvt_f32_f16_e32 v58, v12
	v_cvt_f32_f16_sdwa v59, v12 dst_sel:DWORD dst_unused:UNUSED_PAD src0_sel:WORD_1
	s_waitcnt lgkmcnt(0)
	v_mov_b64_e32 v[50:51], s[20:21]
	s_waitcnt vmcnt(2)
	v_cvt_f32_f16_e32 v56, v16
	v_cvt_f32_f16_sdwa v57, v16 dst_sel:DWORD dst_unused:UNUSED_PAD src0_sel:WORD_1
	v_mad_i64_i32 v[50:51], s[4:5], v35, s16, v[50:51]
	s_waitcnt vmcnt(1)
	v_cvt_f32_f16_e32 v52, v20
	v_cvt_f32_f16_sdwa v53, v20 dst_sel:DWORD dst_unused:UNUSED_PAD src0_sel:WORD_1
	v_fmac_f32_e32 v41, v43, v37
	v_lshl_add_u64 v[46:47], v[50:51], 0, v[46:47]
	s_waitcnt vmcnt(0)
	v_cvt_f32_f16_e32 v50, v24
	v_cvt_f32_f16_sdwa v51, v24 dst_sel:DWORD dst_unused:UNUSED_PAD src0_sel:WORD_1
	v_pk_fma_f32 v[54:55], v[40:41], v[58:59], v[54:55] op_sel_hi:[0,1,1]
	v_fma_f32 v33, -v33, v41, v39
	v_pk_fma_f32 v[54:55], v[38:39], v[56:57], v[54:55] op_sel_hi:[0,1,1]
	v_div_fmas_f32 v33, v33, v37, v41
	v_pk_fma_f32 v[52:53], v[30:31], v[52:53], v[54:55] op_sel_hi:[0,1,1]
	v_cmp_gt_i32_e64 s[0:1], 6, v44
	v_div_fixup_f32 v44, v33, v31, 1.0
	v_pk_fma_f32 v[50:51], v[32:33], v[50:51], v[52:53] op_sel_hi:[0,1,1]
	v_pk_mul_f32 v[50:51], v[44:45], v[50:51] op_sel_hi:[0,1]
	s_waitcnt vmcnt(0) lgkmcnt(0)
	s_mov_b32 s19, s18
	v_pk_fma_f32 v[48:49], s[18:19], v[50:51], v[70:71] op_sel_hi:[0,1,1]
	global_store_dwordx2 v[46:47], v[48:49], off
	s_and_b64 exec, exec, s[0:1]
	s_cbranch_execz .LBB2_3
	v_cvt_f32_f16_sdwa v49, v25 dst_sel:DWORD dst_unused:UNUSED_PAD src0_sel:WORD_1
	v_cvt_f32_f16_e32 v48, v25
	v_cvt_f32_f16_sdwa v25, v21 dst_sel:DWORD dst_unused:UNUSED_PAD src0_sel:WORD_1
	v_cvt_f32_f16_e32 v24, v21
	v_cvt_f32_f16_sdwa v21, v17 dst_sel:DWORD dst_unused:UNUSED_PAD src0_sel:WORD_1
	v_cvt_f32_f16_e32 v20, v17
	v_cvt_f32_f16_sdwa v17, v13 dst_sel:DWORD dst_unused:UNUSED_PAD src0_sel:WORD_1
	v_cvt_f32_f16_e32 v16, v13
	v_cvt_f32_f16_sdwa v13, v26 dst_sel:DWORD dst_unused:UNUSED_PAD src0_sel:WORD_1
	v_cvt_f32_f16_e32 v12, v26
	v_cvt_f32_f16_sdwa v51, v27 dst_sel:DWORD dst_unused:UNUSED_PAD src0_sel:WORD_1
	v_cvt_f32_f16_e32 v50, v27
	v_cvt_f32_f16_sdwa v27, v22 dst_sel:DWORD dst_unused:UNUSED_PAD src0_sel:WORD_1
	v_cvt_f32_f16_e32 v26, v22
	v_cvt_f32_f16_sdwa v53, v23 dst_sel:DWORD dst_unused:UNUSED_PAD src0_sel:WORD_1
	v_cvt_f32_f16_e32 v52, v23
	v_cvt_f32_f16_sdwa v23, v18 dst_sel:DWORD dst_unused:UNUSED_PAD src0_sel:WORD_1
	v_cvt_f32_f16_e32 v22, v18
	v_cvt_f32_f16_sdwa v55, v19 dst_sel:DWORD dst_unused:UNUSED_PAD src0_sel:WORD_1
	v_cvt_f32_f16_e32 v54, v19
	v_cvt_f32_f16_sdwa v19, v14 dst_sel:DWORD dst_unused:UNUSED_PAD src0_sel:WORD_1
	v_cvt_f32_f16_e32 v18, v14
	v_cvt_f32_f16_sdwa v57, v15 dst_sel:DWORD dst_unused:UNUSED_PAD src0_sel:WORD_1
	v_cvt_f32_f16_e32 v56, v15
	v_cvt_f32_f16_sdwa v15, v9 dst_sel:DWORD dst_unused:UNUSED_PAD src0_sel:WORD_1
	v_cvt_f32_f16_e32 v14, v9
	v_cvt_f32_f16_sdwa v9, v10 dst_sel:DWORD dst_unused:UNUSED_PAD src0_sel:WORD_1
	v_cvt_f32_f16_e32 v8, v10
	v_cvt_f32_f16_sdwa v59, v11 dst_sel:DWORD dst_unused:UNUSED_PAD src0_sel:WORD_1
	v_cvt_f32_f16_e32 v58, v11
	v_cvt_f32_f16_sdwa v11, v5 dst_sel:DWORD dst_unused:UNUSED_PAD src0_sel:WORD_1
	v_cvt_f32_f16_e32 v10, v5
	v_cvt_f32_f16_sdwa v5, v6 dst_sel:DWORD dst_unused:UNUSED_PAD src0_sel:WORD_1
	v_cvt_f32_f16_e32 v4, v6
	v_cvt_f32_f16_sdwa v61, v7 dst_sel:DWORD dst_unused:UNUSED_PAD src0_sel:WORD_1
	v_cvt_f32_f16_e32 v60, v7
	v_cvt_f32_f16_sdwa v7, v1 dst_sel:DWORD dst_unused:UNUSED_PAD src0_sel:WORD_1
	v_cvt_f32_f16_e32 v6, v1
	v_cvt_f32_f16_sdwa v1, v2 dst_sel:DWORD dst_unused:UNUSED_PAD src0_sel:WORD_1
	v_cvt_f32_f16_e32 v0, v2
	v_cvt_f32_f16_sdwa v63, v3 dst_sel:DWORD dst_unused:UNUSED_PAD src0_sel:WORD_1
	v_cvt_f32_f16_e32 v62, v3
	v_cndmask_b32_e64 v2, 0, 8, s[0:1]
	v_mov_b32_e32 v3, 0
	v_lshl_add_u64 v[64:65], v[28:29], 0, v[2:3]
	v_cndmask_b32_e64 v2, 0, 16, s[0:1]
	v_mov_b32_e32 v43, v42
	v_lshl_add_u64 v[66:67], v[28:29], 0, v[2:3]
	v_cndmask_b32_e64 v2, 0, 24, s[0:1]
	v_mov_b32_e32 v37, v36
	v_pk_fma_f32 v[6:7], v[42:43], v[6:7], 0 op_sel_hi:[1,1,0]
	v_pk_fma_f32 v[0:1], v[42:43], v[0:1], 0 op_sel_hi:[1,1,0]
	v_lshl_add_u64 v[2:3], v[28:29], 0, v[2:3]
	v_pk_fma_f32 v[6:7], v[36:37], v[10:11], v[6:7]
	v_pk_fma_f32 v[0:1], v[36:37], v[4:5], v[0:1]
	v_pk_fma_f32 v[4:5], v[42:43], v[62:63], 0 op_sel_hi:[1,1,0]
	v_mov_b32_e32 v35, v34
	v_mov_b32_e32 v41, v40
	v_pk_fma_f32 v[2:3], v[36:37], v[60:61], v[4:5]
	v_pk_fma_f32 v[4:5], v[34:35], v[14:15], v[6:7]
	v_pk_fma_f32 v[0:1], v[34:35], v[8:9], v[0:1]
	v_mov_b32_e32 v39, v38
	v_pk_fma_f32 v[2:3], v[34:35], v[58:59], v[2:3]
	v_pk_fma_f32 v[4:5], v[40:41], v[16:17], v[4:5]
	v_pk_fma_f32 v[0:1], v[40:41], v[18:19], v[0:1]
	v_mov_b32_e32 v31, v30
	v_pk_fma_f32 v[2:3], v[40:41], v[56:57], v[2:3]
	v_pk_fma_f32 v[4:5], v[38:39], v[20:21], v[4:5]
	v_pk_fma_f32 v[0:1], v[38:39], v[22:23], v[0:1]
	v_mov_b32_e32 v33, v32
	v_pk_fma_f32 v[6:7], v[38:39], v[54:55], v[2:3]
	v_pk_fma_f32 v[2:3], v[30:31], v[24:25], v[4:5]
	v_pk_fma_f32 v[0:1], v[30:31], v[26:27], v[0:1]
	v_mov_b32_e32 v45, v44
	v_pk_fma_f32 v[2:3], v[32:33], v[48:49], v[2:3]
	v_pk_fma_f32 v[0:1], v[32:33], v[12:13], v[0:1]
	v_pk_mul_f32 v[2:3], v[44:45], v[2:3]
	v_pk_mul_f32 v[4:5], v[44:45], v[0:1]
	v_pk_fma_f32 v[0:1], s[18:19], v[2:3], v[72:73]
	v_pk_fma_f32 v[2:3], s[18:19], v[4:5], v[74:75]
	global_store_dwordx4 v[46:47], v[0:3], off offset:8
	s_nop 1
	v_pk_fma_f32 v[0:1], v[30:31], v[52:53], v[6:7]
	s_nop 0
	v_pk_fma_f32 v[0:1], v[32:33], v[50:51], v[0:1]
	s_nop 0
	v_pk_mul_f32 v[0:1], v[44:45], v[0:1]
	v_pk_fma_f32 v[0:1], s[18:19], v[0:1], v[80:81]
	global_store_dwordx2 v[46:47], v[0:1], off offset:24
